# b1 fragment reads hoisted before the h1 barrier, layer-0 bias patch moved into the previous node's tail, prev hand-off converted to f16 before the lane exchange
# speedup vs baseline: 1.0146x; 1.0146x over previous
.LBB1_2:
	v_lshrrev_b32_e32 v151, 4, v137
	s_lshl_b64 s[6:7], s[2:3], 4
	v_cmp_eq_u32_e64 s[2:3], 1, v151
	s_waitcnt vmcnt(31)
	v_cvt_f16_f32_e32 v8, v8
	v_cmp_gt_u32_e32 vcc, 16, v137
	s_waitcnt vmcnt(29)
	v_cndmask_b32_e64 v116, 0, v116, s[2:3]
	s_waitcnt vmcnt(21)
	v_cndmask_b32_e64 v100, 0, v100, s[2:3]
	v_cmp_eq_u32_e64 s[0:1], 2, v151
	v_cndmask_b32_e64 v114, 0, v114, s[2:3]
	v_cndmask_b32_e64 v115, 0, v115, s[2:3]
	v_cndmask_b32_e32 v6, v116, v6, vcc
	v_cndmask_b32_e64 v116, 0, v117, s[2:3]
	v_cndmask_b32_e64 v108, 0, v108, s[2:3]
	v_cndmask_b32_e32 v26, v100, v26, vcc
	v_cvt_f16_f32_e32 v29, v29
	v_cndmask_b32_e64 v100, 0, v101, s[2:3]
	v_cndmask_b32_e32 v28, 0, v28, vcc
	v_cndmask_b32_e64 v152, 0, 1.0, s[0:1]
	v_cndmask_b32_e32 v114, v114, v120, vcc
	v_cndmask_b32_e32 v115, v115, v121, vcc
	v_cndmask_b32_e32 v7, v116, v7, vcc
	v_cndmask_b32_e64 v106, 0, v106, s[2:3]
	v_cndmask_b32_e64 v107, 0, v107, s[2:3]
	v_cndmask_b32_e32 v14, v108, v14, vcc
	v_cndmask_b32_e64 v108, 0, v109, s[2:3]
	v_cndmask_b32_e32 v27, v100, v27, vcc
	v_cvt_f16_f32_e32 v100, v28
	v_cndmask_b32_e32 v116, 0, v8, vcc
	v_cvt_pk_f16_f32 v8, v6, v7
	v_cvt_pk_f16_f32 v7, v114, v115
	v_cndmask_b32_e64 v114, v152, v140, s[2:3]
	v_cndmask_b32_e32 v106, v106, v112, vcc
	v_cndmask_b32_e32 v107, v107, v113, vcc
	v_cndmask_b32_e32 v15, v108, v15, vcc
	v_cndmask_b32_e64 v98, 0, v98, s[2:3]
	v_cndmask_b32_e64 v99, 0, v99, s[2:3]
	v_cndmask_b32_e32 v110, v114, v110, vcc
	v_cndmask_b32_e64 v114, 0, v141, s[2:3]
	v_cndmask_b32_e32 v108, 0, v16, vcc
	v_cvt_pk_f16_f32 v16, v14, v15
	v_cvt_pk_f16_f32 v15, v106, v107
	v_cndmask_b32_e64 v106, v152, v138, s[2:3]
	v_cndmask_b32_e32 v98, v98, v104, vcc
	v_cndmask_b32_e32 v99, v99, v105, vcc
	v_cndmask_b32_e32 v111, v114, v111, vcc
	v_cndmask_b32_e32 v102, v106, v102, vcc
	v_cndmask_b32_e64 v106, 0, v139, s[2:3]
	v_cndmask_b32_e32 v29, 0, v29, vcc
	v_cvt_pk_f16_f32 v28, v26, v27
	v_cvt_pk_f16_f32 v27, v98, v99
	v_lshlrev_b32_e32 v101, 10, v1
	v_bitop3_b32 v98, v151, v0, 3 bitop3:0x78
	v_lshl_add_u64 v[130:131], s[4:5], 0, v[130:131]
	v_cvt_f16_f32_e32 v4, v4
	v_cvt_pk_f16_f32 v14, v110, v111
	v_cndmask_b32_e32 v103, v106, v103, vcc
	v_pack_b32_f16 v29, v100, v29
	v_lshl_or_b32 v111, v98, 4, v101
	v_lshlrev_b32_e32 v100, 4, v1
	s_movk_i32 s4, 0xc0
	v_cndmask_b32_e64 v124, 0, v124, s[2:3]
	v_cvt_pk_f16_f32 v26, v102, v103
	v_and_b32_e32 v112, 0xc0, v100
	v_bitop3_b32 v100, v100, s4, v111 bitop3:0x26
	s_lshl_b32 s4, s20, 3
	v_lshrrev_b32_e32 v102, 5, v137
	v_lshrrev_b32_e32 v104, 1, v137
	v_cndmask_b32_e64 v122, 0, v122, s[2:3]
	v_cndmask_b32_e64 v123, 0, v123, s[2:3]
	v_cndmask_b32_e32 v2, v124, v2, vcc
	v_cvt_f16_f32_e32 v5, v5
	v_cndmask_b32_e64 v124, 0, v125, s[2:3]
	v_cvt_f16_f32_e32 v9, v9
	v_or_b32_e32 v103, s4, v102
	v_and_or_b32 v110, v104, 8, v101
	v_bitop3_b32 v101, s4, v1, v102 bitop3:0x36
	s_lshl_b32 s4, s20, 4
	v_cndmask_b32_e32 v122, v122, v128, vcc
	v_cndmask_b32_e32 v123, v123, v129, vcc
	v_cndmask_b32_e32 v3, v124, v3, vcc
	v_cndmask_b32_e32 v17, 0, v17, vcc
	v_lshlrev_b32_e32 v107, 4, v101
	v_bitop3_b32 v101, v103, v1, 2 bitop3:0x36
	s_add_i32 s4, s4, 0x10000
	v_bfe_u32 v0, v0, 4, 2
	v_cndmask_b32_e64 v144, v152, v144, s[2:3]
	v_cndmask_b32_e32 v124, 0, v4, vcc
	v_cvt_pk_f16_f32 v4, v2, v3
	v_cvt_pk_f16_f32 v3, v122, v123
	v_cndmask_b32_e64 v122, v152, v142, s[2:3]
	v_cvt_pk_f16_f32 v17, v108, v17
	s_movk_i32 s5, 0x80
	v_lshlrev_b32_e32 v108, 4, v101
	v_bitop3_b32 v101, v103, v1, 4 bitop3:0x36
	s_cmp_lt_u32 s22, 64
	v_lshlrev_b32_e32 v104, 5, v0
	v_lshlrev_b32_e32 v0, 6, v0
	v_cndmask_b32_e32 v126, v144, v126, vcc
	v_cndmask_b32_e64 v144, 0, v145, s[2:3]
	v_cndmask_b32_e32 v118, v122, v118, vcc
	v_cndmask_b32_e64 v122, 0, v143, s[2:3]
	v_bitop3_b32 v99, v112, s5, v111 bitop3:0x36
	v_lshlrev_b32_e32 v109, 4, v101
	v_bitop3_b32 v101, v103, v1, 6 bitop3:0x36
	v_lshl_or_b32 v105, s20, 8, v0
	v_mov_b32_e32 v0, 0x1ec00
	s_cselect_b64 s[4:5], -1, 0
	v_cndmask_b32_e32 v127, v144, v127, vcc
	v_cndmask_b32_e32 v5, 0, v5, vcc
	v_cndmask_b32_e32 v119, v122, v119, vcc
	v_cndmask_b32_e32 v9, 0, v9, vcc
	v_lshlrev_b32_e32 v113, 4, v101
	v_lshlrev_b32_e32 v101, 5, v1
	v_lshl_add_u32 v106, v137, 6, v0
	v_cndmask_b32_e64 v0, 0, 1, s[4:5]
	v_lshl_add_u64 v[132:133], s[8:9], 0, v[132:133]
	v_or_b32_e32 v148, 0x400, v147
	v_or_b32_e32 v149, 0x800, v147
	v_or_b32_e32 v150, 0xc00, v147
	v_cvt_pk_f16_f32 v2, v126, v127
	v_pack_b32_f16 v5, v124, v5
	v_cvt_pk_f16_f32 v6, v118, v119
	v_pack_b32_f16 v9, v116, v9
	v_bitop3_b32 v98, v112, 64, v111 bitop3:0x36
	v_lshl_or_b32 v104, s20, 7, v104
	s_mov_b32 s22, 0x98000
	s_mov_b32 s23, 0x5040100
	s_mov_b32 s24, 0x7060302
	v_add_u32_e32 v107, v107, v110
	v_add_u32_e32 v108, v108, v110
	v_add_u32_e32 v109, v109, v110
	v_add_u32_e32 v110, v113, v110
	v_add_u32_e32 v111, v112, v111
	v_lshlrev_b32_e32 v113, 4, v137
	v_or_b32_e32 v113, 0x10000, v113
	s_lshr_b32 s28, s20, 2
	s_and_b32 s29, s20, 3
	s_lshl_b32 s28, s28, 10
	s_lshl_b32 s29, s29, 2
	s_add_i32 s28, s28, s29
	v_add_u32_e32 v112, s28, v113
	v_cmp_eq_u32_e64 s[26:27], 3, v151
	v_add_u32_e32 v114, 0x12400, v101
	v_cmp_ne_u32_e64 s[4:5], 1, v0
	s_waitcnt vmcnt(16)
	v_cndmask_b32_e64 v1, v30, v134, s[0:1]
	v_bfi_b32 v30, s10, v1, v30
	v_perm_b32 v1, v22, v134, s24
	v_cndmask_b32_e64 v22, v22, v1, s[0:1]
	v_bfi_b32 v1, s10, v135, v18
	v_perm_b32 v121, v10, v135, s24
	v_cndmask_b32_e64 v18, v18, v1, s[0:1]
	v_cndmask_b32_e64 v10, v10, v121, s[0:1]
	v_mov_b32_e32 v121, v136
	v_mov_b32_e32 v144, v136
	v_mov_b32_e32 v145, v136
	v_mov_b32_e32 v0, v136
	v_mov_b32_e32 v1, v136
	s_waitcnt lgkmcnt(0)
	s_barrier
	ds_read_u16 v248, v114
	ds_read_u16 v249, v114 offset:512
	ds_read_u16 v250, v114 offset:1024
	ds_read_u16 v251, v114 offset:1536
	v_add_u32_e32 v114, 2, v114
	s_branch .LBB1_4

.LBB1_4:
	s_waitcnt lgkmcnt(0)
	s_and_saveexec_b64 s[8:9], s[2:3]
	v_perm_b32 v5, v1, v248, s23
	v_perm_b32 v9, v121, v249, s23
	v_perm_b32 v17, v144, v250, s23
	v_perm_b32 v29, v145, v251, s23
	s_or_b64 exec, exec, s[8:9]
	v_add_u32_e32 v0, 0x12c00, v105
	ds_read_b128 v[240:243], v0
	ds_read_b128 v[244:247], v0 offset:16
	ds_read_b128 v[248:251], v0 offset:32
	ds_read_b128 v[252:255], v0 offset:48
	v_mfma_f32_16x16x32_f16 v[126:129], v[30:33], v[6:9], 0
	s_cmp_lg_u32 s22, 0x818000
	v_mfma_f32_16x16x32_f16 v[122:125], v[30:33], v[2:5], 0
	s_cselect_b32 s9, s11, 15
	s_nop 2
	v_cvt_pk_f16_f32 v121, v126, v127
	v_cvt_pk_f16_f32 v127, v128, v129
	v_mfma_f32_16x16x32_f16 v[134:137], v[30:33], v[14:17], 0
	v_pk_max_f16 v126, v121, 0
	s_nop 0
	v_cvt_pk_f16_f32 v0, v122, v123
	v_cvt_pk_f16_f32 v1, v124, v125
	v_mfma_f32_16x16x32_f16 v[30:33], v[30:33], v[26:29], 0
	v_pk_max_f16 v127, v127, 0
	v_pk_max_f16 v0, v0, 0
	v_pk_max_f16 v1, v1, 0
	v_mfma_f32_16x16x32_f16 v[122:125], v[22:25], v[2:5], 0
	ds_write2st64_b64 v107, v[0:1], v[126:127] offset1:32
	s_nop 1
	v_cvt_pk_f16_f32 v0, v134, v135
	v_cvt_pk_f16_f32 v1, v136, v137
	v_mfma_f32_16x16x32_f16 v[126:129], v[22:25], v[6:9], 0
	s_nop 0
	v_cvt_pk_f16_f32 v30, v30, v31
	v_cvt_pk_f16_f32 v31, v32, v33
	v_pk_max_f16 v0, v0, 0
	v_mfma_f32_16x16x32_f16 v[134:137], v[22:25], v[14:17], 0
	v_pk_max_f16 v30, v30, 0
	v_pk_max_f16 v31, v31, 0
	v_pk_max_f16 v1, v1, 0
	v_mfma_f32_16x16x32_f16 v[22:25], v[22:25], v[26:29], 0
	ds_write2st64_b64 v107, v[0:1], v[30:31] offset0:64 offset1:96
	v_cvt_pk_f16_f32 v0, v122, v123
	v_cvt_pk_f16_f32 v1, v124, v125
	v_mfma_f32_16x16x32_f16 v[30:33], v[18:21], v[2:5], 0
	v_pk_max_f16 v0, v0, 0
	v_cvt_pk_f16_f32 v139, v128, v129
	v_pk_max_f16 v1, v1, 0
	v_mfma_f32_16x16x32_f16 v[122:125], v[18:21], v[6:9], 0
	v_cvt_pk_f16_f32 v121, v126, v127
	v_pk_max_f16 v138, v121, 0
	v_pk_max_f16 v139, v139, 0
	v_mfma_f32_16x16x32_f16 v[126:129], v[18:21], v[14:17], 0
	ds_write2st64_b64 v108, v[0:1], v[138:139] offset1:32
	v_cvt_pk_f16_f32 v0, v134, v135
	v_cvt_pk_f16_f32 v1, v136, v137
	v_mfma_f32_16x16x32_f16 v[18:21], v[18:21], v[26:29], 0
	v_pk_max_f16 v0, v0, 0
	v_cvt_pk_f16_f32 v139, v24, v25
	v_pk_max_f16 v1, v1, 0
	v_mfma_f32_16x16x32_f16 v[134:137], v[10:13], v[2:5], 0
	v_cvt_pk_f16_f32 v121, v22, v23
	v_pk_max_f16 v138, v121, 0
	v_pk_max_f16 v139, v139, 0
	ds_write2st64_b64 v108, v[0:1], v[138:139] offset0:64 offset1:96
	v_cvt_pk_f16_f32 v0, v30, v31
	v_mfma_f32_16x16x32_f16 v[22:25], v[10:13], v[6:9], 0
	v_cvt_pk_f16_f32 v1, v32, v33
	v_pk_max_f16 v0, v0, 0
	v_cvt_pk_f16_f32 v30, v122, v123
	v_cvt_pk_f16_f32 v31, v124, v125
	v_mfma_f32_16x16x32_f16 v[138:141], v[10:13], v[14:17], 0
	v_pk_max_f16 v1, v1, 0
	v_pk_max_f16 v30, v30, 0
	v_pk_max_f16 v31, v31, 0
	ds_write2st64_b64 v109, v[0:1], v[30:31] offset1:32
	v_cvt_pk_f16_f32 v0, v126, v127
	v_mfma_f32_16x16x32_f16 v[10:13], v[10:13], v[26:29], 0
	v_cvt_pk_f16_f32 v1, v128, v129
	v_pk_max_f16 v0, v0, 0
	v_cvt_pk_f16_f32 v18, v18, v19
	v_cvt_pk_f16_f32 v19, v20, v21
	v_pk_max_f16 v1, v1, 0
	v_pk_max_f16 v18, v18, 0
	v_pk_max_f16 v19, v19, 0
	ds_write2st64_b64 v109, v[0:1], v[18:19] offset0:64 offset1:96
	v_cvt_pk_f16_f32 v0, v134, v135
	v_cvt_pk_f16_f32 v1, v136, v137
	v_pk_max_f16 v0, v0, 0
	v_cvt_pk_f16_f32 v18, v22, v23
	v_cvt_pk_f16_f32 v19, v24, v25
	v_pk_max_f16 v1, v1, 0
	v_pk_max_f16 v18, v18, 0
	v_pk_max_f16 v19, v19, 0
	ds_write2st64_b64 v110, v[0:1], v[18:19] offset1:32
	v_cvt_pk_f16_f32 v0, v138, v139
	v_cvt_pk_f16_f32 v1, v140, v141
	v_pk_max_f16 v0, v0, 0
	v_cvt_pk_f16_f32 v10, v10, v11
	v_cvt_pk_f16_f32 v11, v12, v13
	v_pk_max_f16 v1, v1, 0
	v_pk_max_f16 v10, v10, 0
	v_pk_max_f16 v11, v11, 0
	ds_write2st64_b64 v110, v[0:1], v[10:11] offset0:64 offset1:96
	s_waitcnt lgkmcnt(0)
	s_barrier
	ds_read_b128 v[122:125], v111
	ds_read_b128 v[126:129], v111 offset:16384
	ds_read_b128 v[134:137], v111 offset:32768
	ds_read_b128 v[138:141], v111 offset:49152
	ds_read_b128 v[142:145], v98
	ds_read_b128 v[152:155], v98 offset:16384
	ds_read_b128 v[156:159], v98 offset:32768
	ds_read_b128 v[160:163], v98 offset:49152
	s_lshl_b32 s20, s9, 7
	v_lshl_add_u64 v[0:1], s[20:21], 3, v[132:133]
	s_add_i32 s25, s22, 0xfff88000
	s_lshl_b32 s8, s9, 8
	buffer_load_dwordx4 v[192:195], v147, s[16:19], s25 offen
	buffer_load_dwordx4 v[196:199], v148, s[16:19], s25 offen
	buffer_load_dwordx4 v[200:203], v149, s[16:19], s25 offen
	buffer_load_dwordx4 v[204:207], v150, s[16:19], s25 offen
	s_waitcnt vmcnt(19) lgkmcnt(7)
	v_mfma_f32_16x16x32_f16 v[164:167], v[58:61], v[122:125], v[240:243]
	s_waitcnt lgkmcnt(6)
	v_mfma_f32_16x16x32_f16 v[168:171], v[58:61], v[126:129], v[240:243]
	s_waitcnt lgkmcnt(5)
	v_mfma_f32_16x16x32_f16 v[172:175], v[58:61], v[134:137], v[240:243]
	s_waitcnt lgkmcnt(4)
	v_mfma_f32_16x16x32_f16 v[10:13], v[58:61], v[138:141], v[240:243]
	s_waitcnt vmcnt(18)
	v_mfma_f32_16x16x32_f16 v[58:61], v[54:57], v[122:125], v[244:247]
	v_mfma_f32_16x16x32_f16 v[176:179], v[54:57], v[126:129], v[244:247]
	v_mfma_f32_16x16x32_f16 v[180:183], v[54:57], v[134:137], v[244:247]
	v_mfma_f32_16x16x32_f16 v[18:21], v[54:57], v[138:141], v[244:247]
	s_waitcnt vmcnt(17)
	v_mfma_f32_16x16x32_f16 v[54:57], v[50:53], v[122:125], v[248:251]
	v_mfma_f32_16x16x32_f16 v[184:187], v[50:53], v[126:129], v[248:251]
	v_mfma_f32_16x16x32_f16 v[188:191], v[50:53], v[134:137], v[248:251]
	v_mfma_f32_16x16x32_f16 v[22:25], v[50:53], v[138:141], v[248:251]
	s_waitcnt vmcnt(16)
	v_mfma_f32_16x16x32_f16 v[50:53], v[38:41], v[122:125], v[252:255]
	v_mfma_f32_16x16x32_f16 v[122:125], v[38:41], v[126:129], v[252:255]
	v_mfma_f32_16x16x32_f16 v[126:129], v[38:41], v[134:137], v[252:255]
	v_mfma_f32_16x16x32_f16 v[38:41], v[38:41], v[138:141], v[252:255]
	ds_read_b128 v[136:139], v99
	ds_read_b128 v[208:211], v99 offset:16384
	ds_read_b128 v[212:215], v99 offset:32768
	ds_read_b128 v[216:219], v99 offset:49152
	s_add_i32 s9, s22, 0xfff90000
	s_waitcnt vmcnt(15) lgkmcnt(7)
	v_mfma_f32_16x16x32_f16 v[164:167], v[94:97], v[142:145], v[164:167]
	s_waitcnt lgkmcnt(6)
	v_mfma_f32_16x16x32_f16 v[168:171], v[94:97], v[152:155], v[168:171]
	s_waitcnt vmcnt(14)
	v_mfma_f32_16x16x32_f16 v[58:61], v[90:93], v[142:145], v[58:61]
	v_mfma_f32_16x16x32_f16 v[176:179], v[90:93], v[152:155], v[176:179]
	s_waitcnt vmcnt(13)
	v_mfma_f32_16x16x32_f16 v[54:57], v[78:81], v[142:145], v[54:57]
	v_mfma_f32_16x16x32_f16 v[184:187], v[78:81], v[152:155], v[184:187]
	s_waitcnt vmcnt(12)
	v_mfma_f32_16x16x32_f16 v[50:53], v[34:37], v[142:145], v[50:53]
	buffer_load_dwordx4 v[140:143], v147, s[16:19], s9 offen
	buffer_load_dwordx4 v[220:223], v148, s[16:19], s9 offen
	v_mfma_f32_16x16x32_f16 v[122:125], v[34:37], v[152:155], v[122:125]
	buffer_load_dwordx4 v[152:155], v149, s[16:19], s9 offen
	buffer_load_dwordx4 v[224:227], v150, s[16:19], s9 offen
	s_mov_b32 s9, s21
	s_waitcnt lgkmcnt(5)
	v_mfma_f32_16x16x32_f16 v[172:175], v[94:97], v[156:159], v[172:175]
	s_waitcnt lgkmcnt(4)
	v_mfma_f32_16x16x32_f16 v[94:97], v[94:97], v[160:163], v[10:13]
	s_nop 2
	v_lshl_add_u64 v[10:11], s[8:9], 4, v[130:131]
	v_mfma_f32_16x16x32_f16 v[180:183], v[90:93], v[156:159], v[180:183]
	v_mfma_f32_16x16x32_f16 v[90:93], v[90:93], v[160:163], v[18:21]
	v_mfma_f32_16x16x32_f16 v[188:191], v[78:81], v[156:159], v[188:191]
	v_mfma_f32_16x16x32_f16 v[78:81], v[78:81], v[160:163], v[22:25]
	global_load_dwordx4 v[30:33], v[10:11], off
	s_nop 1
	global_load_dwordx4 v[22:25], v[10:11], off offset:1024
	global_load_dwordx4 v[18:21], v[10:11], off offset:2048
	s_nop 0
	global_load_dwordx4 v[10:13], v[10:11], off offset:3072
	s_nop 0
	global_load_dwordx2 v[134:135], v[0:1], off
	v_mfma_f32_16x16x32_f16 v[126:129], v[34:37], v[156:159], v[126:129]
	v_mfma_f32_16x16x32_f16 v[34:37], v[34:37], v[160:163], v[38:41]
	s_nop 2
	ds_read_b128 v[38:41], v100
	ds_read_b128 v[156:159], v100 offset:16384
	ds_read_b128 v[160:163], v100 offset:32768
	ds_read_b128 v[228:231], v100 offset:49152
	s_add_i32 s8, s22, 0xfff98000
	s_waitcnt vmcnt(20) lgkmcnt(7)
	v_mfma_f32_16x16x32_f16 v[164:167], v[82:85], v[136:139], v[164:167]
	s_waitcnt lgkmcnt(6)
	v_mfma_f32_16x16x32_f16 v[168:171], v[82:85], v[208:211], v[168:171]
	s_waitcnt lgkmcnt(5)
	v_mfma_f32_16x16x32_f16 v[172:175], v[82:85], v[212:215], v[172:175]
	s_waitcnt lgkmcnt(4)
	v_mfma_f32_16x16x32_f16 v[82:85], v[82:85], v[216:219], v[94:97]
	s_waitcnt vmcnt(19)
	v_mfma_f32_16x16x32_f16 v[58:61], v[70:73], v[136:139], v[58:61]
	v_mfma_f32_16x16x32_f16 v[94:97], v[70:73], v[208:211], v[176:179]
	v_mfma_f32_16x16x32_f16 v[176:179], v[70:73], v[212:215], v[180:183]
	v_mfma_f32_16x16x32_f16 v[70:73], v[70:73], v[216:219], v[90:93]
	s_waitcnt vmcnt(18)
	v_mfma_f32_16x16x32_f16 v[54:57], v[62:65], v[136:139], v[54:57]
	v_mfma_f32_16x16x32_f16 v[90:93], v[62:65], v[208:211], v[184:187]
	v_mfma_f32_16x16x32_f16 v[180:183], v[62:65], v[212:215], v[188:191]
	v_mfma_f32_16x16x32_f16 v[62:65], v[62:65], v[216:219], v[78:81]
	s_waitcnt vmcnt(17)
	v_mfma_f32_16x16x32_f16 v[50:53], v[42:45], v[136:139], v[50:53]
	v_mfma_f32_16x16x32_f16 v[78:81], v[42:45], v[208:211], v[122:125]
	v_mfma_f32_16x16x32_f16 v[122:125], v[42:45], v[212:215], v[126:129]
	s_nop 2
	buffer_load_dwordx4 v[126:129], v147, s[16:19], s8 offen
	buffer_load_dwordx4 v[136:139], v148, s[16:19], s8 offen
	buffer_load_dwordx4 v[184:187], v149, s[16:19], s8 offen
	buffer_load_dwordx4 v[188:191], v150, s[16:19], s8 offen
	v_mfma_f32_16x16x32_f16 v[34:37], v[42:45], v[216:219], v[34:37]
	ds_read_b128 v[42:45], v111 offset:256
	ds_read_b128 v[208:211], v111 offset:16640
	ds_read_b128 v[212:215], v111 offset:33024
	ds_read_b128 v[216:219], v111 offset:49408
	s_add_i32 s8, s22, 0xfffa0000
	s_waitcnt vmcnt(20) lgkmcnt(7)
	v_mfma_f32_16x16x32_f16 v[164:167], v[86:89], v[38:41], v[164:167]
	s_waitcnt lgkmcnt(6)
	v_mfma_f32_16x16x32_f16 v[168:171], v[86:89], v[156:159], v[168:171]
	s_waitcnt lgkmcnt(5)
	v_mfma_f32_16x16x32_f16 v[172:175], v[86:89], v[160:163], v[172:175]
	s_waitcnt lgkmcnt(4)
	v_mfma_f32_16x16x32_f16 v[82:85], v[86:89], v[228:231], v[82:85]
	s_waitcnt vmcnt(19)
	v_mfma_f32_16x16x32_f16 v[58:61], v[74:77], v[38:41], v[58:61]
	v_mfma_f32_16x16x32_f16 v[86:89], v[74:77], v[156:159], v[94:97]
	v_mfma_f32_16x16x32_f16 v[94:97], v[74:77], v[160:163], v[176:179]
	v_mfma_f32_16x16x32_f16 v[70:73], v[74:77], v[228:231], v[70:73]
	s_waitcnt vmcnt(18)
	v_mfma_f32_16x16x32_f16 v[54:57], v[66:69], v[38:41], v[54:57]
	v_mfma_f32_16x16x32_f16 v[74:77], v[66:69], v[156:159], v[90:93]
	v_mfma_f32_16x16x32_f16 v[90:93], v[66:69], v[160:163], v[180:183]
	v_mfma_f32_16x16x32_f16 v[62:65], v[66:69], v[228:231], v[62:65]
	s_waitcnt vmcnt(17)
	v_mfma_f32_16x16x32_f16 v[38:41], v[46:49], v[38:41], v[50:53]
	v_mfma_f32_16x16x32_f16 v[50:53], v[46:49], v[156:159], v[78:81]
	v_mfma_f32_16x16x32_f16 v[66:69], v[46:49], v[160:163], v[122:125]
	s_nop 1
	buffer_load_dwordx4 v[78:81], v147, s[16:19], s8 offen
	buffer_load_dwordx4 v[122:125], v148, s[16:19], s8 offen
	buffer_load_dwordx4 v[156:159], v149, s[16:19], s8 offen
	buffer_load_dwordx4 v[160:163], v150, s[16:19], s8 offen
	v_mfma_f32_16x16x32_f16 v[34:37], v[46:49], v[228:231], v[34:37]
	ds_read_b128 v[46:49], v98 offset:256
	ds_read_b128 v[176:179], v98 offset:16640
	ds_read_b128 v[180:183], v98 offset:33024
	ds_read_b128 v[228:231], v98 offset:49408
	s_add_i32 s8, s22, 0xfffa8000
	s_waitcnt vmcnt(20) lgkmcnt(7)
	v_mfma_f32_16x16x32_f16 v[164:167], v[192:195], v[42:45], v[164:167]
	s_waitcnt lgkmcnt(6)
	v_mfma_f32_16x16x32_f16 v[168:171], v[192:195], v[208:211], v[168:171]
	s_waitcnt lgkmcnt(5)
	v_mfma_f32_16x16x32_f16 v[172:175], v[192:195], v[212:215], v[172:175]
	s_waitcnt lgkmcnt(4)
	v_mfma_f32_16x16x32_f16 v[82:85], v[192:195], v[216:219], v[82:85]
	s_waitcnt vmcnt(19)
	v_mfma_f32_16x16x32_f16 v[58:61], v[196:199], v[42:45], v[58:61]
	v_mfma_f32_16x16x32_f16 v[86:89], v[196:199], v[208:211], v[86:89]
	v_mfma_f32_16x16x32_f16 v[94:97], v[196:199], v[212:215], v[94:97]
	v_mfma_f32_16x16x32_f16 v[70:73], v[196:199], v[216:219], v[70:73]
	s_waitcnt vmcnt(18)
	v_mfma_f32_16x16x32_f16 v[54:57], v[200:203], v[42:45], v[54:57]
	v_mfma_f32_16x16x32_f16 v[74:77], v[200:203], v[208:211], v[74:77]
	v_mfma_f32_16x16x32_f16 v[90:93], v[200:203], v[212:215], v[90:93]
	v_mfma_f32_16x16x32_f16 v[62:65], v[200:203], v[216:219], v[62:65]
	s_waitcnt vmcnt(17)
	v_mfma_f32_16x16x32_f16 v[38:41], v[204:207], v[42:45], v[38:41]
	v_mfma_f32_16x16x32_f16 v[42:45], v[204:207], v[208:211], v[50:53]
	v_mfma_f32_16x16x32_f16 v[50:53], v[204:207], v[212:215], v[66:69]
	s_nop 2
	buffer_load_dwordx4 v[66:69], v147, s[16:19], s8 offen
	buffer_load_dwordx4 v[192:195], v148, s[16:19], s8 offen
	buffer_load_dwordx4 v[196:199], v149, s[16:19], s8 offen
	buffer_load_dwordx4 v[200:203], v150, s[16:19], s8 offen
	v_mfma_f32_16x16x32_f16 v[34:37], v[204:207], v[216:219], v[34:37]
	ds_read_b128 v[204:207], v99 offset:256
	ds_read_b128 v[208:211], v99 offset:16640
	ds_read_b128 v[212:215], v99 offset:33024
	ds_read_b128 v[216:219], v99 offset:49408
	s_add_i32 s8, s22, 0xfffb0000
	s_waitcnt vmcnt(20) lgkmcnt(7)
	v_mfma_f32_16x16x32_f16 v[164:167], v[140:143], v[46:49], v[164:167]
	s_waitcnt lgkmcnt(6)
	v_mfma_f32_16x16x32_f16 v[168:171], v[140:143], v[176:179], v[168:171]
	s_waitcnt lgkmcnt(5)
	v_mfma_f32_16x16x32_f16 v[172:175], v[140:143], v[180:183], v[172:175]
	s_waitcnt lgkmcnt(4)
	v_mfma_f32_16x16x32_f16 v[82:85], v[140:143], v[228:231], v[82:85]
	s_waitcnt vmcnt(19)
	v_mfma_f32_16x16x32_f16 v[58:61], v[220:223], v[46:49], v[58:61]
	v_mfma_f32_16x16x32_f16 v[86:89], v[220:223], v[176:179], v[86:89]
	s_waitcnt vmcnt(18)
	v_mfma_f32_16x16x32_f16 v[54:57], v[152:155], v[46:49], v[54:57]
	v_mfma_f32_16x16x32_f16 v[74:77], v[152:155], v[176:179], v[74:77]
	v_mfma_f32_16x16x32_f16 v[90:93], v[152:155], v[180:183], v[90:93]
	v_mfma_f32_16x16x32_f16 v[62:65], v[152:155], v[228:231], v[62:65]
	s_waitcnt vmcnt(17)
	v_mfma_f32_16x16x32_f16 v[38:41], v[224:227], v[46:49], v[38:41]
	v_mfma_f32_16x16x32_f16 v[42:45], v[224:227], v[176:179], v[42:45]
	v_mfma_f32_16x16x32_f16 v[46:49], v[224:227], v[180:183], v[50:53]
	s_nop 2
	buffer_load_dwordx4 v[50:53], v147, s[16:19], s8 offen
	buffer_load_dwordx4 v[140:143], v148, s[16:19], s8 offen
	buffer_load_dwordx4 v[152:155], v149, s[16:19], s8 offen
	buffer_load_dwordx4 v[176:179], v150, s[16:19], s8 offen
	v_mfma_f32_16x16x32_f16 v[94:97], v[220:223], v[180:183], v[94:97]
	v_mfma_f32_16x16x32_f16 v[70:73], v[220:223], v[228:231], v[70:73]
	v_mfma_f32_16x16x32_f16 v[34:37], v[224:227], v[228:231], v[34:37]
	ds_read_b128 v[180:183], v100 offset:256
	ds_read_b128 v[220:223], v100 offset:16640
	ds_read_b128 v[224:227], v100 offset:33024
	ds_read_b128 v[228:231], v100 offset:49408
	s_add_i32 s8, s22, 0xfffb8000
	s_waitcnt vmcnt(15) lgkmcnt(7)
	v_mfma_f32_16x16x32_f16 v[164:167], v[126:129], v[204:207], v[164:167]
	s_waitcnt lgkmcnt(6)
	v_mfma_f32_16x16x32_f16 v[168:171], v[126:129], v[208:211], v[168:171]
	s_waitcnt lgkmcnt(5)
	v_mfma_f32_16x16x32_f16 v[172:175], v[126:129], v[212:215], v[172:175]
	s_waitcnt lgkmcnt(4)
	v_mfma_f32_16x16x32_f16 v[82:85], v[126:129], v[216:219], v[82:85]
	s_waitcnt vmcnt(14)
	v_mfma_f32_16x16x32_f16 v[58:61], v[136:139], v[204:207], v[58:61]
	v_mfma_f32_16x16x32_f16 v[86:89], v[136:139], v[208:211], v[86:89]
	v_mfma_f32_16x16x32_f16 v[94:97], v[136:139], v[212:215], v[94:97]
	v_mfma_f32_16x16x32_f16 v[70:73], v[136:139], v[216:219], v[70:73]
	s_waitcnt vmcnt(13)
	v_mfma_f32_16x16x32_f16 v[54:57], v[184:187], v[204:207], v[54:57]
	v_mfma_f32_16x16x32_f16 v[74:77], v[184:187], v[208:211], v[74:77]
	v_mfma_f32_16x16x32_f16 v[90:93], v[184:187], v[212:215], v[90:93]
	v_mfma_f32_16x16x32_f16 v[62:65], v[184:187], v[216:219], v[62:65]
	s_waitcnt vmcnt(12)
	v_mfma_f32_16x16x32_f16 v[38:41], v[188:191], v[204:207], v[38:41]
	buffer_load_dwordx4 v[126:129], v147, s[16:19], s8 offen
	buffer_load_dwordx4 v[136:139], v148, s[16:19], s8 offen
	buffer_load_dwordx4 v[184:187], v149, s[16:19], s8 offen
	buffer_load_dwordx4 v[204:207], v150, s[16:19], s8 offen
	v_mfma_f32_16x16x32_f16 v[42:45], v[188:191], v[208:211], v[42:45]
	v_mfma_f32_16x16x32_f16 v[46:49], v[188:191], v[212:215], v[46:49]
	v_mfma_f32_16x16x32_f16 v[34:37], v[188:191], v[216:219], v[34:37]
	ds_read_b128 v[188:191], v111 offset:512
	ds_read_b128 v[208:211], v111 offset:16896
	ds_read_b128 v[212:215], v111 offset:33280
	ds_read_b128 v[216:219], v111 offset:49664
	s_add_i32 s8, s22, 0xfffc0000
	s_waitcnt vmcnt(15) lgkmcnt(7)
	v_mfma_f32_16x16x32_f16 v[164:167], v[78:81], v[180:183], v[164:167]
	s_waitcnt lgkmcnt(6)
	v_mfma_f32_16x16x32_f16 v[168:171], v[78:81], v[220:223], v[168:171]
	s_waitcnt lgkmcnt(5)
	v_mfma_f32_16x16x32_f16 v[172:175], v[78:81], v[224:227], v[172:175]
	s_waitcnt lgkmcnt(4)
	v_mfma_f32_16x16x32_f16 v[78:81], v[78:81], v[228:231], v[82:85]
	s_waitcnt vmcnt(14)
	v_mfma_f32_16x16x32_f16 v[58:61], v[122:125], v[180:183], v[58:61]
	v_mfma_f32_16x16x32_f16 v[82:85], v[122:125], v[220:223], v[86:89]
	v_mfma_f32_16x16x32_f16 v[86:89], v[122:125], v[224:227], v[94:97]
	v_mfma_f32_16x16x32_f16 v[70:73], v[122:125], v[228:231], v[70:73]
	s_waitcnt vmcnt(13)
	v_mfma_f32_16x16x32_f16 v[54:57], v[156:159], v[180:183], v[54:57]
	v_mfma_f32_16x16x32_f16 v[74:77], v[156:159], v[220:223], v[74:77]
	v_mfma_f32_16x16x32_f16 v[90:93], v[156:159], v[224:227], v[90:93]
	v_mfma_f32_16x16x32_f16 v[62:65], v[156:159], v[228:231], v[62:65]
	s_waitcnt vmcnt(12)
	v_mfma_f32_16x16x32_f16 v[38:41], v[160:163], v[180:183], v[38:41]
	buffer_load_dwordx4 v[94:97], v147, s[16:19], s8 offen
	buffer_load_dwordx4 v[122:125], v148, s[16:19], s8 offen
	buffer_load_dwordx4 v[156:159], v149, s[16:19], s8 offen
	buffer_load_dwordx4 v[180:183], v150, s[16:19], s8 offen
	v_mfma_f32_16x16x32_f16 v[42:45], v[160:163], v[220:223], v[42:45]
	v_mfma_f32_16x16x32_f16 v[46:49], v[160:163], v[224:227], v[46:49]
	v_mfma_f32_16x16x32_f16 v[34:37], v[160:163], v[228:231], v[34:37]
	ds_read_b128 v[160:163], v98 offset:512
	ds_read_b128 v[220:223], v98 offset:16896
	ds_read_b128 v[224:227], v98 offset:33280
	ds_read_b128 v[228:231], v98 offset:49664
	s_add_i32 s8, s22, 0xfffc8000
	s_waitcnt vmcnt(15) lgkmcnt(7)
	v_mfma_f32_16x16x32_f16 v[164:167], v[66:69], v[188:191], v[164:167]
	s_waitcnt lgkmcnt(6)
	v_mfma_f32_16x16x32_f16 v[168:171], v[66:69], v[208:211], v[168:171]
	s_waitcnt lgkmcnt(5)
	v_mfma_f32_16x16x32_f16 v[172:175], v[66:69], v[212:215], v[172:175]
	s_waitcnt lgkmcnt(4)
	v_mfma_f32_16x16x32_f16 v[66:69], v[66:69], v[216:219], v[78:81]
	s_waitcnt vmcnt(14)
	v_mfma_f32_16x16x32_f16 v[58:61], v[192:195], v[188:191], v[58:61]
	v_mfma_f32_16x16x32_f16 v[78:81], v[192:195], v[208:211], v[82:85]
	v_mfma_f32_16x16x32_f16 v[82:85], v[192:195], v[212:215], v[86:89]
	v_mfma_f32_16x16x32_f16 v[70:73], v[192:195], v[216:219], v[70:73]
	s_waitcnt vmcnt(13)
	v_mfma_f32_16x16x32_f16 v[54:57], v[196:199], v[188:191], v[54:57]
	v_mfma_f32_16x16x32_f16 v[74:77], v[196:199], v[208:211], v[74:77]
	v_mfma_f32_16x16x32_f16 v[86:89], v[196:199], v[212:215], v[90:93]
	v_mfma_f32_16x16x32_f16 v[62:65], v[196:199], v[216:219], v[62:65]
	s_waitcnt vmcnt(12)
	v_mfma_f32_16x16x32_f16 v[38:41], v[200:203], v[188:191], v[38:41]
	buffer_load_dwordx4 v[90:93], v147, s[16:19], s8 offen
	buffer_load_dwordx4 v[188:191], v148, s[16:19], s8 offen
	buffer_load_dwordx4 v[192:195], v149, s[16:19], s8 offen
	buffer_load_dwordx4 v[196:199], v150, s[16:19], s8 offen
	v_mfma_f32_16x16x32_f16 v[42:45], v[200:203], v[208:211], v[42:45]
	v_mfma_f32_16x16x32_f16 v[46:49], v[200:203], v[212:215], v[46:49]
	v_mfma_f32_16x16x32_f16 v[34:37], v[200:203], v[216:219], v[34:37]
	ds_read_b128 v[200:203], v99 offset:512
	ds_read_b128 v[208:211], v99 offset:16896
	ds_read_b128 v[212:215], v99 offset:33280
	ds_read_b128 v[216:219], v99 offset:49664
	s_add_i32 s8, s22, 0xfffd0000
	s_waitcnt vmcnt(15) lgkmcnt(7)
	v_mfma_f32_16x16x32_f16 v[164:167], v[50:53], v[160:163], v[164:167]
	s_waitcnt lgkmcnt(6)
	v_mfma_f32_16x16x32_f16 v[168:171], v[50:53], v[220:223], v[168:171]
	s_waitcnt lgkmcnt(5)
	v_mfma_f32_16x16x32_f16 v[172:175], v[50:53], v[224:227], v[172:175]
	s_waitcnt lgkmcnt(4)
	v_mfma_f32_16x16x32_f16 v[50:53], v[50:53], v[228:231], v[66:69]
	s_waitcnt vmcnt(14)
	v_mfma_f32_16x16x32_f16 v[58:61], v[140:143], v[160:163], v[58:61]
	v_mfma_f32_16x16x32_f16 v[66:69], v[140:143], v[220:223], v[78:81]
	v_mfma_f32_16x16x32_f16 v[78:81], v[140:143], v[224:227], v[82:85]
	v_mfma_f32_16x16x32_f16 v[70:73], v[140:143], v[228:231], v[70:73]
	s_waitcnt vmcnt(13)
	v_mfma_f32_16x16x32_f16 v[54:57], v[152:155], v[160:163], v[54:57]
	v_mfma_f32_16x16x32_f16 v[74:77], v[152:155], v[220:223], v[74:77]
	v_mfma_f32_16x16x32_f16 v[82:85], v[152:155], v[224:227], v[86:89]
	v_mfma_f32_16x16x32_f16 v[62:65], v[152:155], v[228:231], v[62:65]
	s_waitcnt vmcnt(12)
	v_mfma_f32_16x16x32_f16 v[38:41], v[176:179], v[160:163], v[38:41]
	buffer_load_dwordx4 v[86:89], v147, s[16:19], s8 offen
	buffer_load_dwordx4 v[140:143], v148, s[16:19], s8 offen
	buffer_load_dwordx4 v[152:155], v149, s[16:19], s8 offen
	buffer_load_dwordx4 v[160:163], v150, s[16:19], s8 offen
	v_mfma_f32_16x16x32_f16 v[42:45], v[176:179], v[220:223], v[42:45]
	v_mfma_f32_16x16x32_f16 v[46:49], v[176:179], v[224:227], v[46:49]
	v_mfma_f32_16x16x32_f16 v[34:37], v[176:179], v[228:231], v[34:37]
	ds_read_b128 v[176:179], v100 offset:512
	ds_read_b128 v[220:223], v100 offset:16896
	ds_read_b128 v[224:227], v100 offset:33280
	ds_read_b128 v[228:231], v100 offset:49664
	s_add_i32 s8, s22, 0xfffd8000
	s_waitcnt vmcnt(15) lgkmcnt(7)
	v_mfma_f32_16x16x32_f16 v[164:167], v[126:129], v[200:203], v[164:167]
	s_waitcnt lgkmcnt(6)
	v_mfma_f32_16x16x32_f16 v[168:171], v[126:129], v[208:211], v[168:171]
	s_waitcnt lgkmcnt(5)
	v_mfma_f32_16x16x32_f16 v[172:175], v[126:129], v[212:215], v[172:175]
	s_waitcnt lgkmcnt(4)
	v_mfma_f32_16x16x32_f16 v[50:53], v[126:129], v[216:219], v[50:53]
	s_waitcnt vmcnt(14)
	v_mfma_f32_16x16x32_f16 v[58:61], v[136:139], v[200:203], v[58:61]
	v_mfma_f32_16x16x32_f16 v[66:69], v[136:139], v[208:211], v[66:69]
	v_mfma_f32_16x16x32_f16 v[78:81], v[136:139], v[212:215], v[78:81]
	v_mfma_f32_16x16x32_f16 v[70:73], v[136:139], v[216:219], v[70:73]
	s_waitcnt vmcnt(13)
	v_mfma_f32_16x16x32_f16 v[54:57], v[184:187], v[200:203], v[54:57]
	v_mfma_f32_16x16x32_f16 v[74:77], v[184:187], v[208:211], v[74:77]
	v_mfma_f32_16x16x32_f16 v[82:85], v[184:187], v[212:215], v[82:85]
	v_mfma_f32_16x16x32_f16 v[62:65], v[184:187], v[216:219], v[62:65]
	s_waitcnt vmcnt(12)
	v_mfma_f32_16x16x32_f16 v[38:41], v[204:207], v[200:203], v[38:41]
	buffer_load_dwordx4 v[126:129], v147, s[16:19], s8 offen
	buffer_load_dwordx4 v[136:139], v148, s[16:19], s8 offen
	buffer_load_dwordx4 v[184:187], v149, s[16:19], s8 offen
	buffer_load_dwordx4 v[200:203], v150, s[16:19], s8 offen
	v_mfma_f32_16x16x32_f16 v[42:45], v[204:207], v[208:211], v[42:45]
	v_mfma_f32_16x16x32_f16 v[46:49], v[204:207], v[212:215], v[46:49]
	v_mfma_f32_16x16x32_f16 v[34:37], v[204:207], v[216:219], v[34:37]
	ds_read_b128 v[204:207], v111 offset:768
	ds_read_b128 v[208:211], v111 offset:17152
	ds_read_b128 v[212:215], v111 offset:33536
	ds_read_b128 v[216:219], v111 offset:49920
	s_add_i32 s8, s22, 0xfffe0000
	s_waitcnt vmcnt(15) lgkmcnt(7)
	v_mfma_f32_16x16x32_f16 v[164:167], v[94:97], v[176:179], v[164:167]
	s_waitcnt lgkmcnt(6)
	v_mfma_f32_16x16x32_f16 v[168:171], v[94:97], v[220:223], v[168:171]
	s_waitcnt vmcnt(14)
	v_mfma_f32_16x16x32_f16 v[58:61], v[122:125], v[176:179], v[58:61]
	v_mfma_f32_16x16x32_f16 v[66:69], v[122:125], v[220:223], v[66:69]
	s_waitcnt lgkmcnt(5)
	v_mfma_f32_16x16x32_f16 v[78:81], v[122:125], v[224:227], v[78:81]
	s_waitcnt lgkmcnt(4)
	v_mfma_f32_16x16x32_f16 v[70:73], v[122:125], v[228:231], v[70:73]
	s_waitcnt vmcnt(13)
	v_mfma_f32_16x16x32_f16 v[54:57], v[156:159], v[176:179], v[54:57]
	v_mfma_f32_16x16x32_f16 v[74:77], v[156:159], v[220:223], v[74:77]
	v_mfma_f32_16x16x32_f16 v[82:85], v[156:159], v[224:227], v[82:85]
	v_mfma_f32_16x16x32_f16 v[62:65], v[156:159], v[228:231], v[62:65]
	s_waitcnt vmcnt(12)
	v_mfma_f32_16x16x32_f16 v[38:41], v[180:183], v[176:179], v[38:41]
	v_mfma_f32_16x16x32_f16 v[42:45], v[180:183], v[220:223], v[42:45]
	buffer_load_dwordx4 v[122:125], v147, s[16:19], s8 offen
	buffer_load_dwordx4 v[156:159], v148, s[16:19], s8 offen
	buffer_load_dwordx4 v[176:179], v149, s[16:19], s8 offen
	buffer_load_dwordx4 v[220:223], v150, s[16:19], s8 offen
	v_mfma_f32_16x16x32_f16 v[50:53], v[94:97], v[228:231], v[50:53]
	v_mfma_f32_16x16x32_f16 v[46:49], v[180:183], v[224:227], v[46:49]
	v_mfma_f32_16x16x32_f16 v[34:37], v[180:183], v[228:231], v[34:37]
	v_mfma_f32_16x16x32_f16 v[172:175], v[94:97], v[224:227], v[172:175]
	ds_read_b128 v[94:97], v98 offset:768
	ds_read_b128 v[180:183], v98 offset:17152
	ds_read_b128 v[224:227], v98 offset:33536
	ds_read_b128 v[228:231], v98 offset:49920
	s_add_i32 s8, s22, 0xfffe8000
	s_waitcnt vmcnt(15) lgkmcnt(7)
	v_mfma_f32_16x16x32_f16 v[164:167], v[90:93], v[204:207], v[164:167]
	s_waitcnt lgkmcnt(6)
	v_mfma_f32_16x16x32_f16 v[168:171], v[90:93], v[208:211], v[168:171]
	s_waitcnt lgkmcnt(5)
	v_mfma_f32_16x16x32_f16 v[172:175], v[90:93], v[212:215], v[172:175]
	s_waitcnt lgkmcnt(4)
	v_mfma_f32_16x16x32_f16 v[90:93], v[90:93], v[216:219], v[50:53]
	s_waitcnt vmcnt(14)
	v_mfma_f32_16x16x32_f16 v[232:235], v[188:191], v[204:207], v[58:61]
	v_mfma_f32_16x16x32_f16 v[66:69], v[188:191], v[208:211], v[66:69]
	v_mfma_f32_16x16x32_f16 v[78:81], v[188:191], v[212:215], v[78:81]
	v_mfma_f32_16x16x32_f16 v[70:73], v[188:191], v[216:219], v[70:73]
	s_waitcnt vmcnt(13)
	v_mfma_f32_16x16x32_f16 v[188:191], v[192:195], v[204:207], v[54:57]
	v_mfma_f32_16x16x32_f16 v[74:77], v[192:195], v[208:211], v[74:77]
	v_mfma_f32_16x16x32_f16 v[82:85], v[192:195], v[212:215], v[82:85]
	v_mfma_f32_16x16x32_f16 v[62:65], v[192:195], v[216:219], v[62:65]
	s_waitcnt vmcnt(12)
	v_mfma_f32_16x16x32_f16 v[192:195], v[196:199], v[204:207], v[38:41]
	buffer_load_dwordx4 v[58:61], v147, s[16:19], s8 offen
	buffer_load_dwordx4 v[54:57], v148, s[16:19], s8 offen
	buffer_load_dwordx4 v[50:53], v149, s[16:19], s8 offen
	buffer_load_dwordx4 v[38:41], v150, s[16:19], s8 offen
	v_mfma_f32_16x16x32_f16 v[42:45], v[196:199], v[208:211], v[42:45]
	v_mfma_f32_16x16x32_f16 v[46:49], v[196:199], v[212:215], v[46:49]
	v_mfma_f32_16x16x32_f16 v[196:199], v[196:199], v[216:219], v[34:37]
	ds_read_b128 v[204:207], v99 offset:768
	ds_read_b128 v[208:211], v99 offset:17152
	ds_read_b128 v[212:215], v99 offset:33536
	ds_read_b128 v[216:219], v99 offset:49920
	s_add_i32 s8, s22, 0xffff0000
	s_waitcnt vmcnt(15) lgkmcnt(7)
	v_mfma_f32_16x16x32_f16 v[164:167], v[86:89], v[94:97], v[164:167]
	s_waitcnt lgkmcnt(6)
	v_mfma_f32_16x16x32_f16 v[168:171], v[86:89], v[180:183], v[168:171]
	s_waitcnt lgkmcnt(5)
	v_mfma_f32_16x16x32_f16 v[172:175], v[86:89], v[224:227], v[172:175]
	s_waitcnt lgkmcnt(4)
	v_mfma_f32_16x16x32_f16 v[86:89], v[86:89], v[228:231], v[90:93]
	s_waitcnt vmcnt(14)
	v_mfma_f32_16x16x32_f16 v[232:235], v[140:143], v[94:97], v[232:235]
	v_mfma_f32_16x16x32_f16 v[66:69], v[140:143], v[180:183], v[66:69]
	v_mfma_f32_16x16x32_f16 v[236:239], v[140:143], v[224:227], v[78:81]
	v_mfma_f32_16x16x32_f16 v[70:73], v[140:143], v[228:231], v[70:73]
	s_waitcnt vmcnt(13)
	v_mfma_f32_16x16x32_f16 v[140:143], v[152:155], v[94:97], v[188:191]
	v_mfma_f32_16x16x32_f16 v[74:77], v[152:155], v[180:183], v[74:77]
	v_mfma_f32_16x16x32_f16 v[82:85], v[152:155], v[224:227], v[82:85]
	v_mfma_f32_16x16x32_f16 v[62:65], v[152:155], v[228:231], v[62:65]
	s_waitcnt vmcnt(12)
	v_mfma_f32_16x16x32_f16 v[152:155], v[160:163], v[94:97], v[192:195]
	buffer_load_dwordx4 v[94:97], v147, s[16:19], s8 offen
	buffer_load_dwordx4 v[90:93], v148, s[16:19], s8 offen
	buffer_load_dwordx4 v[78:81], v149, s[16:19], s8 offen
	buffer_load_dwordx4 v[34:37], v150, s[16:19], s8 offen
	v_mfma_f32_16x16x32_f16 v[42:45], v[160:163], v[180:183], v[42:45]
	v_mfma_f32_16x16x32_f16 v[46:49], v[160:163], v[224:227], v[46:49]
	v_mfma_f32_16x16x32_f16 v[160:163], v[160:163], v[228:231], v[196:199]
	ds_read_b128 v[180:183], v100 offset:768
	ds_read_b128 v[188:191], v100 offset:17152
	ds_read_b128 v[192:195], v100 offset:33536
	ds_read_b128 v[196:199], v100 offset:49920
	s_add_i32 s8, s22, 0xffff8000
	s_waitcnt vmcnt(15) lgkmcnt(7)
	v_mfma_f32_16x16x32_f16 v[164:167], v[126:129], v[204:207], v[164:167]
	s_waitcnt lgkmcnt(6)
	v_mfma_f32_16x16x32_f16 v[168:171], v[126:129], v[208:211], v[168:171]
	s_waitcnt lgkmcnt(5)
	v_mfma_f32_16x16x32_f16 v[172:175], v[126:129], v[212:215], v[172:175]
	s_waitcnt lgkmcnt(4)
	v_mfma_f32_16x16x32_f16 v[86:89], v[126:129], v[216:219], v[86:89]
	s_waitcnt vmcnt(14)
	v_mfma_f32_16x16x32_f16 v[126:129], v[136:139], v[204:207], v[232:235]
	v_mfma_f32_16x16x32_f16 v[66:69], v[136:139], v[208:211], v[66:69]
	v_mfma_f32_16x16x32_f16 v[224:227], v[136:139], v[212:215], v[236:239]
	v_mfma_f32_16x16x32_f16 v[136:139], v[136:139], v[216:219], v[70:73]
	s_waitcnt vmcnt(13)
	v_mfma_f32_16x16x32_f16 v[140:143], v[184:187], v[204:207], v[140:143]
	v_mfma_f32_16x16x32_f16 v[74:77], v[184:187], v[208:211], v[74:77]
	v_mfma_f32_16x16x32_f16 v[228:231], v[184:187], v[212:215], v[82:85]
	v_mfma_f32_16x16x32_f16 v[184:187], v[184:187], v[216:219], v[62:65]
	s_waitcnt vmcnt(12)
	v_mfma_f32_16x16x32_f16 v[152:155], v[200:203], v[204:207], v[152:155]
	v_mfma_f32_16x16x32_f16 v[204:207], v[200:203], v[208:211], v[42:45]
	buffer_load_dwordx4 v[82:85], v147, s[16:19], s8 offen
	buffer_load_dwordx4 v[70:73], v148, s[16:19], s8 offen
	buffer_load_dwordx4 v[62:65], v149, s[16:19], s8 offen
	buffer_load_dwordx4 v[42:45], v150, s[16:19], s8 offen
	v_mfma_f32_16x16x32_f16 v[46:49], v[200:203], v[212:215], v[46:49]
	v_mfma_f32_16x16x32_f16 v[160:163], v[200:203], v[216:219], v[160:163]
	v_add_u32_e32 v0, 0x1ac00, v104
	ds_read_b128 v[240:243], v0
	ds_read_b128 v[244:247], v0 offset:16
	s_waitcnt vmcnt(12) lgkmcnt(5)
	v_mfma_f32_16x16x32_f16 v[164:167], v[122:125], v[180:183], v[164:167]
	v_mfma_f32_16x16x32_f16 v[126:129], v[156:159], v[180:183], v[126:129]
	v_mfma_f32_16x16x32_f16 v[140:143], v[176:179], v[180:183], v[140:143]
	v_mfma_f32_16x16x32_f16 v[152:155], v[220:223], v[180:183], v[152:155]
	s_waitcnt lgkmcnt(4)
	v_mfma_f32_16x16x32_f16 v[168:171], v[122:125], v[188:191], v[168:171]
	v_mfma_f32_16x16x32_f16 v[208:211], v[156:159], v[188:191], v[66:69]
	v_mfma_f32_16x16x32_f16 v[212:215], v[176:179], v[188:191], v[74:77]
	v_mfma_f32_16x16x32_f16 v[204:207], v[220:223], v[188:191], v[204:207]
	s_waitcnt lgkmcnt(3)
	v_mfma_f32_16x16x32_f16 v[172:175], v[122:125], v[192:195], v[172:175]
	v_cvt_pk_f16_f32 v232, v164, v165
	v_cvt_pk_f16_f32 v233, v166, v167
	v_pk_max_f16 v232, v232, 0
	v_pk_max_f16 v233, v233, 0
	v_mfma_f32_16x16x32_f16 v[224:227], v[156:159], v[192:195], v[224:227]
	v_cvt_pk_f16_f32 v234, v126, v127
	v_cvt_pk_f16_f32 v235, v128, v129
	v_pk_max_f16 v234, v234, 0
	v_pk_max_f16 v235, v235, 0
	v_mfma_f32_16x16x32_f16 v[228:231], v[176:179], v[192:195], v[228:231]
	v_cvt_pk_f16_f32 v236, v140, v141
	v_cvt_pk_f16_f32 v237, v142, v143
	v_pk_max_f16 v236, v236, 0
	v_pk_max_f16 v237, v237, 0
	v_mfma_f32_16x16x32_f16 v[216:219], v[220:223], v[192:195], v[46:49]
	v_cvt_pk_f16_f32 v238, v152, v153
	v_cvt_pk_f16_f32 v239, v154, v155
	v_pk_max_f16 v238, v238, 0
	v_pk_max_f16 v239, v239, 0
	s_waitcnt lgkmcnt(2)
	v_mfma_f32_16x16x32_f16 v[200:203], v[122:125], v[196:199], v[86:89]
	v_cvt_pk_f16_f32 v180, v168, v169
	v_cvt_pk_f16_f32 v181, v170, v171
	v_pk_max_f16 v180, v180, 0
	v_pk_max_f16 v181, v181, 0
	buffer_load_dwordx4 v[86:89], v147, s[16:19], s22 offen
	buffer_load_dwordx4 v[74:77], v148, s[16:19], s22 offen
	buffer_load_dwordx4 v[66:69], v149, s[16:19], s22 offen
	buffer_load_dwordx4 v[46:49], v150, s[16:19], s22 offen
	v_mfma_f32_16x16x32_f16 v[136:139], v[156:159], v[196:199], v[136:139]
	v_cvt_pk_f16_f32 v182, v208, v209
	v_cvt_pk_f16_f32 v183, v210, v211
	v_pk_max_f16 v182, v182, 0
	v_pk_max_f16 v183, v183, 0
	s_waitcnt lgkmcnt(1)
	v_mfma_f32_16x16x32_f16 v[252:255], v[240:243], v[232:235], 0
	v_mfma_f32_16x16x32_f16 v[184:187], v[176:179], v[196:199], v[184:187]
	v_cvt_pk_f16_f32 v188, v212, v213
	v_cvt_pk_f16_f32 v189, v214, v215
	v_pk_max_f16 v188, v188, 0
	v_pk_max_f16 v189, v189, 0
	s_waitcnt lgkmcnt(0)
	v_mfma_f32_16x16x32_f16 v[252:255], v[244:247], v[236:239], v[252:255]
	v_mfma_f32_16x16x32_f16 v[160:163], v[220:223], v[196:199], v[160:163]
	v_cvt_pk_f16_f32 v190, v204, v205
	v_cvt_pk_f16_f32 v191, v206, v207
	v_pk_max_f16 v190, v190, 0
	v_pk_max_f16 v191, v191, 0
	v_cvt_pk_f16_f32 v232, v172, v173
	v_cvt_pk_f16_f32 v233, v174, v175
	v_pk_max_f16 v232, v232, 0
	v_pk_max_f16 v233, v233, 0
	v_cvt_pk_f16_f32 v234, v224, v225
	v_cvt_pk_f16_f32 v235, v226, v227
	v_pk_max_f16 v234, v234, 0
	v_pk_max_f16 v235, v235, 0
	v_mfma_f32_16x16x32_f16 v[192:195], v[240:243], v[180:183], 0
	v_cvt_pk_f16_f32 v236, v228, v229
	v_cvt_pk_f16_f32 v237, v230, v231
	v_pk_max_f16 v236, v236, 0
	v_pk_max_f16 v237, v237, 0
	v_mfma_f32_16x16x32_f16 v[192:195], v[244:247], v[188:191], v[192:195]
	v_cvt_pk_f16_f32 v238, v216, v217
	v_cvt_pk_f16_f32 v239, v218, v219
	v_pk_max_f16 v238, v238, 0
	v_pk_max_f16 v239, v239, 0
	v_cvt_pk_f16_f32 v180, v200, v201
	v_cvt_pk_f16_f32 v181, v202, v203
	v_pk_max_f16 v180, v180, 0
	v_pk_max_f16 v181, v181, 0
	v_mfma_f32_16x16x32_f16 v[196:199], v[240:243], v[232:235], 0
	v_cvt_pk_f16_f32 v182, v136, v137
	v_cvt_pk_f16_f32 v183, v138, v139
	v_pk_max_f16 v182, v182, 0
	v_pk_max_f16 v183, v183, 0
	v_mfma_f32_16x16x32_f16 v[196:199], v[244:247], v[236:239], v[196:199]
	v_cvt_pk_f16_f32 v188, v184, v185
	v_cvt_pk_f16_f32 v189, v186, v187
	v_pk_max_f16 v188, v188, 0
	v_pk_max_f16 v189, v189, 0
	v_cvt_pk_f16_f32 v190, v160, v161
	v_cvt_pk_f16_f32 v191, v162, v163
	v_pk_max_f16 v190, v190, 0
	v_pk_max_f16 v191, v191, 0
	v_mfma_f32_16x16x32_f16 v[122:125], v[240:243], v[180:183], 0
	s_nop 0
	v_mfma_f32_16x16x32_f16 v[122:125], v[244:247], v[188:191], v[122:125]
	s_load_dword s30, s[12:13], 0x0
	v_cndmask_b32_e64 v0, v252, v192, s[2:3]
	v_cndmask_b32_e64 v0, v0, v196, s[0:1]
	s_waitcnt vmcnt(16)
	v_cndmask_b32_e64 v1, v30, v134, s[0:1]
	v_bfi_b32 v30, s10, v1, v30
	v_perm_b32 v1, v22, v134, s24
	v_cndmask_b32_e64 v22, v22, v1, s[0:1]
	v_bfi_b32 v1, s10, v135, v18
	v_perm_b32 v121, v10, v135, s24
	v_cndmask_b32_e64 v18, v18, v1, s[0:1]
	v_cndmask_b32_e64 v10, v10, v121, s[0:1]
	v_cndmask_b32_e64 v0, v0, v122, s[26:27]
	ds_write_b32 v112, v0
	s_waitcnt lgkmcnt(0)
	s_barrier
	ds_read_b128 v[232:235], v113
	ds_read_b128 v[236:239], v113 offset:1024
	ds_read_u16 v248, v114
	ds_read_u16 v249, v114 offset:512
	ds_read_u16 v250, v114 offset:1024
	ds_read_u16 v251, v114 offset:1536
	s_and_b64 vcc, exec, s[4:5]
	s_waitcnt lgkmcnt(4)
	v_add_f32_e32 v0, v232, v233
	v_add_f32_e32 v1, v234, v235
	v_add_f32_e32 v121, v236, v237
	v_add_f32_e32 v144, v238, v239
	v_add_f32_e32 v0, v0, v1
	v_add_f32_e32 v121, v121, v144
	v_add_f32_e32 v0, v0, v121
	v_add_f32_e32 v0, s30, v0
	s_cbranch_vccnz .Lskip_out
	ds_write_b32 v106, v0
.Lskip_out:
	v_cvt_f16_f32_e32 v1, v0
	v_cvt_f16_f32_e32 v121, v0
	s_nop 1
	v_permlane16_swap_b32_e32 v1, v121
	v_mov_b32_e32 v144, v1
	v_mov_b32_e32 v145, v121
	s_nop 1
	v_permlane32_swap_b32_e32 v1, v144
	v_permlane32_swap_b32_e32 v121, v145
	s_branch .LBB1_3

amdhsa.kernels:
  - .agpr_count:     0
    .args:
      - .actual_access:  read_only
        .address_space:  global
        .offset:         0
        .size:           8
        .value_kind:     global_buffer
      - .actual_access:  write_only
        .address_space:  global
        .offset:         8
        .size:           8
        .value_kind:     global_buffer
      - .actual_access:  read_only
        .address_space:  global
        .offset:         16
        .size:           8
        .value_kind:     global_buffer
      - .actual_access:  read_only
        .address_space:  global
        .offset:         24
        .size:           8
        .value_kind:     global_buffer
      - .actual_access:  read_only
        .address_space:  global
        .offset:         32
        .size:           8
        .value_kind:     global_buffer
      - .actual_access:  read_only
        .address_space:  global
        .offset:         40
        .size:           8
        .value_kind:     global_buffer
      - .actual_access:  read_only
        .address_space:  global
        .offset:         48
        .size:           8
        .value_kind:     global_buffer
      - .actual_access:  read_only
        .address_space:  global
        .offset:         56
        .size:           8
        .value_kind:     global_buffer
      - .actual_access:  read_only
        .address_space:  global
        .offset:         64
        .size:           8
        .value_kind:     global_buffer
      - .actual_access:  read_only
        .address_space:  global
        .offset:         72
        .size:           8
        .value_kind:     global_buffer
      - .actual_access:  read_only
        .address_space:  global
        .offset:         80
        .size:           8
        .value_kind:     global_buffer
      - .actual_access:  write_only
        .address_space:  global
        .offset:         88
        .size:           8
        .value_kind:     global_buffer
      - .actual_access:  write_only
        .address_space:  global
        .offset:         96
        .size:           8
        .value_kind:     global_buffer
      - .actual_access:  write_only
        .address_space:  global
        .offset:         104
        .size:           8
        .value_kind:     global_buffer
      - .actual_access:  write_only
        .address_space:  global
        .offset:         112
        .size:           8
        .value_kind:     global_buffer
      - .actual_access:  write_only
        .address_space:  global
        .offset:         120
        .size:           8
        .value_kind:     global_buffer
    .group_segment_fixed_size: 17440
    .kernarg_segment_align: 8
    .kernarg_segment_size: 128
    .language:       OpenCL C
    .language_version:
      - 2
      - 0
    .max_flat_workgroup_size: 256
    .name:           _Z11prep_kernelPKfPDv8_DF16_S0_S0_S0_S0_S0_S0_S0_S0_S0_S2_PfPDF16_S4_S3_
    .private_segment_fixed_size: 0
    .sgpr_count:     32
    .sgpr_spill_count: 0
    .symbol:         _Z11prep_kernelPKfPDv8_DF16_S0_S0_S0_S0_S0_S0_S0_S0_S0_S2_PfPDF16_S4_S3_.kd
    .uniform_work_group_size: 1
    .uses_dynamic_stack: false
    .vgpr_count:     42
    .vgpr_spill_count: 0
    .wavefront_size: 64
  - .agpr_count:     0
    .args:
      - .actual_access:  read_only
        .address_space:  global
        .offset:         0
        .size:           8
        .value_kind:     global_buffer
      - .actual_access:  read_only
        .address_space:  global
        .offset:         8
        .size:           8
        .value_kind:     global_buffer
      - .actual_access:  read_only
        .address_space:  global
        .offset:         16
        .size:           8
        .value_kind:     global_buffer
      - .actual_access:  read_only
        .address_space:  global
        .offset:         24
        .size:           8
        .value_kind:     global_buffer
      - .actual_access:  read_only
        .address_space:  global
        .offset:         32
        .size:           8
        .value_kind:     global_buffer
      - .actual_access:  read_only
        .address_space:  global
        .offset:         40
        .size:           8
        .value_kind:     global_buffer
      - .actual_access:  read_only
        .address_space:  global
        .offset:         48
        .size:           8
        .value_kind:     global_buffer
      - .actual_access:  read_only
        .address_space:  global
        .offset:         56
        .size:           8
        .value_kind:     global_buffer
      - .actual_access:  read_only
        .address_space:  global
        .offset:         64
        .size:           8
        .value_kind:     global_buffer
      - .actual_access:  write_only
        .address_space:  global
        .offset:         72
        .size:           8
        .value_kind:     global_buffer
    .group_segment_fixed_size: 130304
    .kernarg_segment_align: 8
    .kernarg_segment_size: 80
    .language:       OpenCL C
    .language_version:
      - 2
      - 0
    .max_flat_workgroup_size: 512
    .name:           _Z16pdag_main_kernelPKfS0_S0_PKDv8_DF16_S3_S0_PKDF16_S5_S0_Pf
    .private_segment_fixed_size: 0
    .sgpr_count:     72
    .sgpr_spill_count: 0
    .symbol:         _Z16pdag_main_kernelPKfS0_S0_PKDv8_DF16_S3_S0_PKDF16_S5_S0_Pf.kd
    .uniform_work_group_size: 1
    .uses_dynamic_stack: false
    .vgpr_count:     256
    .vgpr_spill_count: 0
    .wavefront_size: 64
